# FFN1 unit walk order: (pn-half, pm, pn-low) so a round of 32 units per XCD covers 4 row tiles x 8 weight tiles (3 MB working set) instead of 2 x 16 (weights alone fill the 4 MB L2)
# speedup vs baseline: 1.0039x; 1.0030x over previous
.LBB0_1908:
	v_readlane_b32 s78, v254, 2
	v_readlane_b32 s79, v254, 3
	v_readlane_b32 s72, v254, 10
	v_lshrrev_b32_e32 v2, 6, v0
	s_nop 4
	s_load_dwordx2 s[80:81], s[78:79], 0x100
	s_load_dwordx2 s[78:79], s[78:79], 0x118
	v_readfirstlane_b32 s32, v2
	s_waitcnt lgkmcnt(0)
	s_lshl_b32 s72, s72, 27
	s_add_u32 s80, s80, s72
	s_addc_u32 s81, s81, 0
	s_and_b32 s72, s32, 1
	s_lshl_b32 s72, s72, 17
	s_add_u32 s80, s80, s72
	s_addc_u32 s81, s81, 0
	s_add_u32 s78, s78, 0x9bb0000
	s_addc_u32 s79, s79, 0
	s_and_b32 s72, s32, 1
	s_lshl_b32 s72, s72, 5
	s_add_u32 s78, s78, s72
	s_addc_u32 s79, s79, 0
	s_lshr_b32 s72, s32, 1
	s_lshl_b32 s72, s72, 8
	s_load_dword s32, s[96:97], 0x0
	s_waitcnt lgkmcnt(0)
	s_cmpk_lg_u32 s32, 0x100
	s_cselect_b32 s72, 0x7fff0000, s72
	v_writelane_b32 v255, s80, 40
	v_writelane_b32 v255, s81, 41
	v_writelane_b32 v255, s78, 42
	v_writelane_b32 v255, s79, 43
	v_writelane_b32 v255, s72, 44
	s_mov_b32 s32, 0
	v_readlane_b32 s8, v255, 3
	v_readlane_b32 s9, v255, 4
	s_and_b64 s[8:9], s[8:9], exec
	v_readlane_b32 s0, v254, 2
	s_cselect_b32 s3, 16, 17
	v_readlane_b32 s1, v254, 3
	v_mov_b32_e32 v2, v0
	s_lshl_b32 s8, s3, 8
	s_mov_b32 s6, s2
	s_cmp_ge_i32 s6, s8
	v_readfirstlane_b32 s10, v2
	s_cbranch_scc1 .LBB0_1922
	s_waitcnt vmcnt(0)
	v_ashrrev_i32_e32 v5, 31, v2
	v_lshrrev_b32_e32 v5, 26, v5
	v_add_u32_e32 v5, v2, v5
	v_ashrrev_i32_e32 v12, 6, v5
	v_bfe_i32 v5, v2, 27, 1
	v_lshlrev_b32_e32 v4, 4, v2
	v_lshrrev_b32_e32 v5, 22, v5
	v_add_u32_e32 v5, v4, v5
	v_and_b32_e32 v5, 0xfffffc00, v5
	v_sub_u32_e32 v5, v4, v5
	v_lshrrev_b32_e32 v6, 4, v5
	s_load_dwordx2 s[38:39], s[0:1], 0x118
	v_bitop3_b32 v13, v6, v5, 32 bitop3:0x6c
	v_ashrrev_i32_e32 v5, 31, v5
	v_lshrrev_b32_e32 v5, 26, v5
	v_add_u32_e32 v5, v13, v5
	v_add_u32_e32 v4, 0x2000, v4
	v_ashrrev_i32_e32 v14, 6, v5
	v_ashrrev_i32_e32 v5, 31, v4
	v_lshrrev_b32_e32 v5, 22, v5
	s_waitcnt lgkmcnt(0)
	s_add_u32 s26, s38, 0x163b0000
	v_add_u32_e32 v5, v4, v5
	s_addc_u32 s27, s39, 0
	v_ashrrev_i32_e32 v15, 10, v5
	s_add_u32 s11, s38, 0x1bb0000
	v_mul_i32_i24_e32 v5, 0x400, v15
	s_addc_u32 s12, s39, 0
	v_sub_u32_e32 v4, v4, v5
	s_add_u32 s21, s38, 0x233f0000
	v_lshrrev_b32_e32 v5, 4, v4
	s_addc_u32 s25, s39, 0
	v_bitop3_b32 v16, v5, v4, 32 bitop3:0x6c
	v_lshlrev_b32_e32 v5, 3, v12
	s_lshl_b32 s59, s3, 4
	v_and_b32_e32 v5, -16, v5
	s_abs_i32 s60, s59
	v_add_u32_e32 v6, v14, v5
	v_cvt_f32_u32_e32 v5, s60
	s_ashr_i32 s9, s6, 31
	s_lshr_b32 s9, s9, 29
	s_add_i32 s9, s6, s9
	v_rcp_iflag_f32_e32 v5, v5
	s_ashr_i32 s36, s9, 3
	s_and_b32 s9, s9, -8
	s_sub_i32 s6, s6, s9
	v_mul_f32_e32 v5, 0x4f7ffffe, v5
	v_cvt_u32_f32_e32 v5, v5
	s_lshl_b32 s58, s3, 5
	s_lshr_b32 s9, s6, 31
	s_or_b32 s9, s9, s58
	s_mul_i32 s6, s9, s6
	s_add_i32 s6, s6, s36
	s_sub_i32 s36, 0, s60
	v_readfirstlane_b32 s62, v5
	s_mul_i32 s36, s36, s62
	s_ashr_i32 s9, s6, 31
	s_bfe_i32 s61, s3, 0x1001b
	s_mul_hi_u32 s36, s62, s36
	s_xor_b32 s3, s9, s61
	s_abs_i32 s9, s6
	s_add_i32 s62, s62, s36
	s_mul_hi_u32 s36, s9, s62
	s_mul_i32 s37, s36, s60
	s_ashr_i32 s1, s10, 6
	s_sub_i32 s9, s9, s37
	s_ashr_i32 s0, s10, 8
	s_lshl_b32 s56, s1, 10
	s_add_i32 s37, s36, 1
	s_sub_i32 s40, s9, s60
	s_cmp_ge_u32 s9, s60
	s_cselect_b32 s36, s37, s36
	s_cselect_b32 s9, s40, s9
	s_add_i32 s37, s36, 1
	s_cmp_ge_u32 s9, s60
	s_cselect_b32 s9, s37, s36
	s_xor_b32 s9, s9, s3
	s_sub_i32 s40, s9, s3
	s_mul_i32 s3, s40, s59
	s_sub_i32 s3, s6, s3
	s_lshr_b32 s9, s59, 1
	s_cmp_ge_u32 s3, s9
	s_cselect_b32 s36, s9, 0
	s_cselect_b32 s37, 8, 0
	s_sub_i32 s3, s3, s36
	s_and_b32 s36, s3, 7
	s_lshr_b32 s3, s3, 3
	s_lshl_b32 s3, s3, 4
	s_or_b32 s3, s3, s36
	s_or_b32 s3, s3, s37
	s_bfe_u32 s9, s3, 0x4001b
	s_add_i32 s9, s3, s9
	s_sext_i32_i16 s36, s9
	v_ashrrev_i32_e32 v4, 31, v16
	s_mul_i32 s6, s40, 17
	s_ashr_i32 s36, s36, 4
	v_lshrrev_b32_e32 v4, 26, v4
	s_add_i32 s48, s6, s36
	v_add_u32_e32 v17, v16, v4
	v_lshlrev_b32_e32 v4, 3, v15
	s_and_b32 s6, s9, 0xfff0
	s_ashr_i32 s49, s48, 31
	v_ashrrev_i32_e32 v18, 6, v17
	v_and_b32_e32 v4, -16, v4
	s_sub_i32 s42, s3, s6
	s_lshl_b64 s[36:37], s[48:49], 10
	v_add_u32_e32 v4, v18, v4
	s_add_u32 s36, s21, s36
	s_addc_u32 s37, s25, s37
	v_ashrrev_i32_e32 v7, 31, v6
	v_ashrrev_i32_e32 v5, 31, v4
	v_mov_b32_e32 v117, 0x7a7a7a7a
	v_mov_b32_e32 v198, 0x7f7f7f7f
	v_lshl_add_u64 v[8:9], v[6:7], 2, s[36:37]
	v_lshl_add_u64 v[10:11], v[4:5], 2, s[36:37]
	s_load_dword s57, s[96:97], 0x0
	global_load_dword v19, v[8:9], off
	global_load_dword v20, v[10:11], off
	s_nop 0
	global_load_dword v10, v[10:11], off offset:512
	s_nop 0
	global_load_dword v8, v[8:9], off offset:512
	v_mul_i32_i24_e32 v11, 64, v14
	v_sub_u32_e32 v11, v13, v11
	v_lshlrev_b32_e32 v9, 5, v12
	v_ashrrev_i16_sdwa v11, v250, sext(v11) dst_sel:DWORD dst_unused:UNUSED_PAD src0_sel:DWORD src1_sel:BYTE_0
	v_and_b32_e32 v9, 32, v9
	v_bfe_i32 v11, v11, 0, 16
	v_add_lshl_u32 v199, v9, v11, 1
	v_and_b32_e32 v11, 0xc0, v17
	v_sub_u32_e32 v11, v16, v11
	v_lshlrev_b32_e32 v9, 5, v15
	v_ashrrev_i16_sdwa v11, v250, sext(v11) dst_sel:DWORD dst_unused:UNUSED_PAD src0_sel:DWORD src1_sel:BYTE_0
	v_and_b32_e32 v9, 32, v9
	v_bfe_i32 v11, v11, 0, 16
	v_add_lshl_u32 v200, v9, v11, 1
	v_and_b32_e32 v9, 3, v18
	s_mov_b32 s3, 0x3fffe0
	v_lshrrev_b32_e32 v11, 2, v4
	v_lshlrev_b32_e32 v12, 1, v4
	v_and_or_b32 v9, v4, s3, v9
	v_and_b32_e32 v11, 4, v11
	v_and_b32_e32 v12, 24, v12
	v_or3_b32 v9, v9, v11, v12
	s_ashr_i32 s41, s40, 31
	v_lshl_add_u32 v166, v9, 10, v200
	v_and_b32_e32 v9, 3, v14
	s_lshl_b64 s[40:41], s[40:41], 22
	v_and_or_b32 v9, v6, s3, v9
	s_add_u32 s3, s11, s40
	s_addc_u32 s6, s12, s41
	s_bfe_i64 s[40:41], s[42:43], 0x100000
	v_lshrrev_b32_e32 v11, 2, v6
	v_lshlrev_b32_e32 v12, 1, v6
	s_lshl_b64 s[40:41], s[40:41], 18
	v_and_b32_e32 v11, 4, v11
	v_and_b32_e32 v12, 24, v12
	s_add_u32 s50, s3, s40
	v_or3_b32 v9, v9, v11, v12
	s_addc_u32 s51, s6, s41
	s_add_i32 s49, s56, 0
	v_lshl_add_u32 v168, v9, 10, v199
	s_add_i32 m0, s49, 0x10400
	s_add_i32 s63, s49, 0x400
	global_load_lds_dwordx4 v168, s[50:51]
	s_add_i32 m0, s49, 0x12400
	s_add_i32 s64, s49, 0x2400
	global_load_lds_dwordx4 v166, s[50:51]
	s_mov_b32 m0, s63
	s_add_u32 s40, s50, 0x20000
	s_addc_u32 s41, s51, 0
	s_add_i32 s65, s49, 0x4400
	s_add_i32 s66, s49, 0x6400
	v_mov_b32_e32 v169, v3
	v_mov_b32_e32 v167, v3
	v_mov_b32_e32 v185, v3
	v_mov_b32_e32 v181, v3
	v_lshl_add_u64 v[14:15], s[50:51], 0, v[168:169]
	v_lshl_add_u64 v[12:13], s[50:51], 0, v[166:167]
	s_waitcnt vmcnt(0)
	v_lshl_add_u32 v184, v19, 10, v199
	v_lshl_add_u32 v180, v20, 10, v200
	global_load_lds_dwordx4 v184, s[26:27]
	s_mov_b32 m0, s64
	v_lshl_add_u32 v178, v8, 10, v199
	global_load_lds_dwordx4 v180, s[26:27]
	s_add_i32 m0, s49, 0x14400
	v_lshl_add_u32 v176, v10, 10, v200
	global_load_lds_dwordx4 v168, s[40:41]
	s_add_i32 m0, s49, 0x16400
	v_lshl_add_u64 v[10:11], s[26:27], 0, v[184:185]
	global_load_lds_dwordx4 v166, s[40:41]
	s_mov_b32 m0, s65
	s_cmp_lg_u32 s0, 1
	global_load_lds_dwordx4 v178, s[26:27]
	s_mov_b32 m0, s66
	v_lshl_add_u64 v[8:9], s[26:27], 0, v[180:181]
	global_load_lds_dwordx4 v176, s[26:27]
	s_cbranch_scc1 .LBB0_1911
	s_barrier

.LBB0_1913:
	s_add_i32 s69, s69, 1
	s_mov_b32 s6, s2
	s_waitcnt lgkmcnt(0)
	s_mul_i32 s0, s69, s57
	s_ashr_i32 s38, s6, 31
	s_mul_hi_u32 s1, s69, s57
	s_add_u32 s0, s0, s6
	s_addc_u32 s1, s1, s38
	v_mov_b64_e32 v[4:5], s[8:9]
	v_cmp_ge_i64_e64 s[38:39], s[0:1], v[4:5]
	s_and_b64 vcc, exec, s[38:39]
	s_cbranch_vccnz .LBB0_1915
	s_ashr_i32 s1, s0, 31
	s_lshr_b32 s1, s1, 29
	s_add_i32 s1, s0, s1
	s_ashr_i32 s6, s1, 3
	s_and_b32 s1, s1, -8
	s_sub_i32 s0, s0, s1
	s_lshr_b32 s1, s0, 31
	s_or_b32 s1, s1, s58
	s_mul_i32 s0, s1, s0
	s_add_i32 s1, s0, s6
	s_abs_i32 s6, s1
	s_mul_hi_u32 s36, s6, s62
	s_mul_i32 s37, s36, s60
	s_ashr_i32 s0, s1, 31
	s_sub_i32 s6, s6, s37
	s_xor_b32 s0, s0, s61
	s_add_i32 s37, s36, 1
	s_sub_i32 s42, s6, s60
	s_cmp_ge_u32 s6, s60
	s_cselect_b32 s36, s37, s36
	s_cselect_b32 s6, s42, s6
	s_add_i32 s37, s36, 1
	s_cmp_ge_u32 s6, s60
	s_cselect_b32 s6, s37, s36
	s_xor_b32 s6, s6, s0
	s_sub_i32 s0, s6, s0
	s_mul_i32 s6, s0, s59
	s_sub_i32 s1, s1, s6
	s_lshr_b32 s36, s59, 1
	s_cmp_ge_u32 s1, s36
	s_cselect_b32 s37, s36, 0
	s_cselect_b32 s6, 8, 0
	s_sub_i32 s1, s1, s37
	s_and_b32 s37, s1, 7
	s_lshr_b32 s1, s1, 3
	s_lshl_b32 s1, s1, 4
	s_or_b32 s1, s1, s37
	s_or_b32 s1, s1, s6
	s_ashr_i32 s36, s1, 31
	s_lshr_b32 s36, s36, 28
	s_add_i32 s36, s1, s36
	s_mul_i32 s6, s0, 17
	s_ashr_i32 s37, s36, 4
	s_add_i32 s42, s37, s6
	s_and_b32 s6, s36, -16
	s_ashr_i32 s43, s42, 31
	s_sub_i32 s44, s1, s6
	s_lshl_b64 s[36:37], s[42:43], 10
	s_add_u32 s36, s21, s36
	s_addc_u32 s37, s25, s37
	s_ashr_i32 s1, s0, 31
	s_lshl_b64 s[0:1], s[0:1], 22
	s_add_u32 s6, s11, s0
	s_addc_u32 s43, s12, s1
	s_ashr_i32 s45, s44, 31
	s_lshl_b64 s[0:1], s[44:45], 18
	s_add_u32 s46, s6, s0
	s_addc_u32 s47, s43, s1
